# gemm: balanced read split + LDS-DMAs moved to the read-free MFMA gaps (slots 9,12,15 of each block)
# baseline (speedup 1.0000x reference)
.Lgemm_T_loop:
	s_waitcnt lgkmcnt(0)
	ds_read_b128 v[146:149], v164
	v_mfma_f32_16x16x32_f16 v[82:85], v[134:137], v[86:89], v[82:85]
	ds_read_b128 v[150:153], v164 offset:2048
	v_mfma_f32_16x16x32_f16 v[58:61], v[138:141], v[86:89], v[58:61]
	ds_read_b128 v[154:157], v164 offset:4096
	v_mfma_f32_16x16x32_f16 v[14:17], v[142:145], v[86:89], v[14:17]
	ds_read_b128 v[110:113], v160
	v_mfma_f32_16x16x32_f16 v[78:81], v[134:137], v[90:93], v[78:81]
	ds_read_b128 v[114:117], v160 offset:2048
	v_mfma_f32_16x16x32_f16 v[22:25], v[138:141], v[90:93], v[22:25]
	ds_read_b128 v[118:121], v160 offset:4096
	v_mfma_f32_16x16x32_f16 v[30:33], v[142:145], v[90:93], v[30:33]
	ds_read_b128 v[122:125], v160 offset:6144
	v_mfma_f32_16x16x32_f16 v[74:77], v[134:137], v[94:97], v[74:77]
	ds_read_b128 v[126:129], v160 offset:8192
	v_mfma_f32_16x16x32_f16 v[18:21], v[138:141], v[94:97], v[18:21]
	ds_read_b128 v[130:133], v160 offset:10240
	v_mfma_f32_16x16x32_f16 v[26:29], v[142:145], v[94:97], v[26:29]
	s_add_u32 m0, s11, 0x1e080
	v_mfma_f32_16x16x32_f16 v[70:73], v[134:137], v[98:101], v[70:73]
	global_load_lds_dwordx4 v[220:221], off offset:-128
	v_mfma_f32_16x16x32_f16 v[46:49], v[138:141], v[98:101], v[46:49]
	v_mfma_f32_16x16x32_f16 v[240:243], v[142:145], v[98:101], v[240:243]
	s_add_u32 m0, s11, 0x20080
	v_mfma_f32_16x16x32_f16 v[66:69], v[134:137], v[102:105], v[66:69]
	global_load_lds_dwordx4 v[224:225], off offset:-128
	v_mfma_f32_16x16x32_f16 v[42:45], v[138:141], v[102:105], v[42:45]
	v_mfma_f32_16x16x32_f16 v[236:239], v[142:145], v[102:105], v[236:239]
	s_add_u32 m0, s11, 0x22080
	v_mfma_f32_16x16x32_f16 v[62:65], v[134:137], v[106:109], v[62:65]
	global_load_lds_dwordx4 v[228:229], off offset:-128
	v_mfma_f32_16x16x32_f16 v[38:41], v[138:141], v[106:109], v[38:41]
	v_mfma_f32_16x16x32_f16 v[34:37], v[142:145], v[106:109], v[34:37]
	s_waitcnt vmcnt(6) lgkmcnt(0)
	s_barrier
	ds_read_b128 v[134:137], v162 offset:49152
	v_mfma_f32_16x16x32_f16 v[82:85], v[146:149], v[110:113], v[82:85]
	ds_read_b128 v[138:141], v162 offset:51200
	v_mfma_f32_16x16x32_f16 v[58:61], v[150:153], v[110:113], v[58:61]
	ds_read_b128 v[142:145], v162 offset:53248
	v_mfma_f32_16x16x32_f16 v[14:17], v[154:157], v[110:113], v[14:17]
	ds_read_b128 v[86:89], v158 offset:49152
	v_mfma_f32_16x16x32_f16 v[78:81], v[146:149], v[114:117], v[78:81]
	ds_read_b128 v[90:93], v158 offset:51200
	v_mfma_f32_16x16x32_f16 v[22:25], v[150:153], v[114:117], v[22:25]
	ds_read_b128 v[94:97], v158 offset:53248
	v_mfma_f32_16x16x32_f16 v[30:33], v[154:157], v[114:117], v[30:33]
	ds_read_b128 v[98:101], v158 offset:55296
	v_mfma_f32_16x16x32_f16 v[74:77], v[146:149], v[118:121], v[74:77]
	ds_read_b128 v[102:105], v158 offset:57344
	v_mfma_f32_16x16x32_f16 v[18:21], v[150:153], v[118:121], v[18:21]
	ds_read_b128 v[106:109], v158 offset:59392
	v_mfma_f32_16x16x32_f16 v[26:29], v[154:157], v[118:121], v[26:29]
	s_add_u32 m0, s11, 0x0
	v_mfma_f32_16x16x32_f16 v[70:73], v[146:149], v[122:125], v[70:73]
	global_load_lds_dwordx4 v[218:219], off
	v_mfma_f32_16x16x32_f16 v[46:49], v[150:153], v[122:125], v[46:49]
	v_mfma_f32_16x16x32_f16 v[240:243], v[154:157], v[122:125], v[240:243]
	s_add_u32 m0, s11, 0x2000
	v_mfma_f32_16x16x32_f16 v[66:69], v[146:149], v[126:129], v[66:69]
	global_load_lds_dwordx4 v[222:223], off
	v_mfma_f32_16x16x32_f16 v[42:45], v[150:153], v[126:129], v[42:45]
	v_mfma_f32_16x16x32_f16 v[236:239], v[154:157], v[126:129], v[236:239]
	s_add_u32 m0, s11, 0x4000
	v_mfma_f32_16x16x32_f16 v[62:65], v[146:149], v[130:133], v[62:65]
	global_load_lds_dwordx4 v[226:227], off
	v_mfma_f32_16x16x32_f16 v[38:41], v[150:153], v[130:133], v[38:41]
	v_mfma_f32_16x16x32_f16 v[34:37], v[154:157], v[130:133], v[34:37]
	s_waitcnt lgkmcnt(0)
	ds_read_b128 v[146:149], v164 offset:49152
	v_mfma_f32_16x16x32_f16 v[82:85], v[134:137], v[86:89], v[82:85]
	ds_read_b128 v[150:153], v164 offset:51200
	v_mfma_f32_16x16x32_f16 v[58:61], v[138:141], v[86:89], v[58:61]
	ds_read_b128 v[154:157], v164 offset:53248
	v_mfma_f32_16x16x32_f16 v[14:17], v[142:145], v[86:89], v[14:17]
	ds_read_b128 v[110:113], v160 offset:49152
	v_mfma_f32_16x16x32_f16 v[78:81], v[134:137], v[90:93], v[78:81]
	ds_read_b128 v[114:117], v160 offset:51200
	v_mfma_f32_16x16x32_f16 v[22:25], v[138:141], v[90:93], v[22:25]
	ds_read_b128 v[118:121], v160 offset:53248
	v_mfma_f32_16x16x32_f16 v[30:33], v[142:145], v[90:93], v[30:33]
	ds_read_b128 v[122:125], v160 offset:55296
	v_mfma_f32_16x16x32_f16 v[74:77], v[134:137], v[94:97], v[74:77]
	ds_read_b128 v[126:129], v160 offset:57344
	v_mfma_f32_16x16x32_f16 v[18:21], v[138:141], v[94:97], v[18:21]
	ds_read_b128 v[130:133], v160 offset:59392
	v_mfma_f32_16x16x32_f16 v[26:29], v[142:145], v[94:97], v[26:29]
	s_add_u32 m0, s11, 0x6000
	v_mfma_f32_16x16x32_f16 v[70:73], v[134:137], v[98:101], v[70:73]
	global_load_lds_dwordx4 v[220:221], off
	v_mfma_f32_16x16x32_f16 v[46:49], v[138:141], v[98:101], v[46:49]
	v_mfma_f32_16x16x32_f16 v[240:243], v[142:145], v[98:101], v[240:243]
	s_add_u32 m0, s11, 0x8000
	v_mfma_f32_16x16x32_f16 v[66:69], v[134:137], v[102:105], v[66:69]
	global_load_lds_dwordx4 v[224:225], off
	v_mfma_f32_16x16x32_f16 v[42:45], v[138:141], v[102:105], v[42:45]
	v_mfma_f32_16x16x32_f16 v[236:239], v[142:145], v[102:105], v[236:239]
	s_add_u32 m0, s11, 0xa000
	v_mfma_f32_16x16x32_f16 v[62:65], v[134:137], v[106:109], v[62:65]
	global_load_lds_dwordx4 v[228:229], off
	v_mfma_f32_16x16x32_f16 v[38:41], v[138:141], v[106:109], v[38:41]
	v_mfma_f32_16x16x32_f16 v[34:37], v[142:145], v[106:109], v[34:37]
	s_waitcnt vmcnt(6) lgkmcnt(0)
	s_barrier
	ds_read_b128 v[134:137], v163
	v_mfma_f32_16x16x32_f16 v[82:85], v[146:149], v[110:113], v[82:85]
	ds_read_b128 v[138:141], v163 offset:2048
	v_mfma_f32_16x16x32_f16 v[58:61], v[150:153], v[110:113], v[58:61]
	ds_read_b128 v[142:145], v163 offset:4096
	v_mfma_f32_16x16x32_f16 v[14:17], v[154:157], v[110:113], v[14:17]
	ds_read_b128 v[86:89], v159
	v_mfma_f32_16x16x32_f16 v[78:81], v[146:149], v[114:117], v[78:81]
	ds_read_b128 v[90:93], v159 offset:2048
	v_mfma_f32_16x16x32_f16 v[22:25], v[150:153], v[114:117], v[22:25]
	ds_read_b128 v[94:97], v159 offset:4096
	v_mfma_f32_16x16x32_f16 v[30:33], v[154:157], v[114:117], v[30:33]
	ds_read_b128 v[98:101], v159 offset:6144
	v_mfma_f32_16x16x32_f16 v[74:77], v[146:149], v[118:121], v[74:77]
	ds_read_b128 v[102:105], v159 offset:8192
	v_mfma_f32_16x16x32_f16 v[18:21], v[150:153], v[118:121], v[18:21]
	ds_read_b128 v[106:109], v159 offset:10240
	v_mfma_f32_16x16x32_f16 v[26:29], v[154:157], v[118:121], v[26:29]
	s_add_u32 m0, s11, 0xbf80
	v_mfma_f32_16x16x32_f16 v[70:73], v[146:149], v[122:125], v[70:73]
	global_load_lds_dwordx4 v[218:219], off offset:128
	v_mfma_f32_16x16x32_f16 v[46:49], v[150:153], v[122:125], v[46:49]
	v_mfma_f32_16x16x32_f16 v[240:243], v[154:157], v[122:125], v[240:243]
	s_add_u32 m0, s11, 0xdf80
	v_mfma_f32_16x16x32_f16 v[66:69], v[146:149], v[126:129], v[66:69]
	global_load_lds_dwordx4 v[222:223], off offset:128
	v_mfma_f32_16x16x32_f16 v[42:45], v[150:153], v[126:129], v[42:45]
	v_mfma_f32_16x16x32_f16 v[236:239], v[154:157], v[126:129], v[236:239]
	s_add_u32 m0, s11, 0xff80
	v_mfma_f32_16x16x32_f16 v[62:65], v[146:149], v[130:133], v[62:65]
	global_load_lds_dwordx4 v[226:227], off offset:128
	v_mfma_f32_16x16x32_f16 v[38:41], v[150:153], v[130:133], v[38:41]
	v_mfma_f32_16x16x32_f16 v[34:37], v[154:157], v[130:133], v[34:37]
	s_waitcnt lgkmcnt(0)
	ds_read_b128 v[146:149], v165
	v_mfma_f32_16x16x32_f16 v[82:85], v[134:137], v[86:89], v[82:85]
	ds_read_b128 v[150:153], v165 offset:2048
	v_mfma_f32_16x16x32_f16 v[58:61], v[138:141], v[86:89], v[58:61]
	ds_read_b128 v[154:157], v165 offset:4096
	v_mfma_f32_16x16x32_f16 v[14:17], v[142:145], v[86:89], v[14:17]
	ds_read_b128 v[110:113], v161
	v_mfma_f32_16x16x32_f16 v[78:81], v[134:137], v[90:93], v[78:81]
	ds_read_b128 v[114:117], v161 offset:2048
	v_mfma_f32_16x16x32_f16 v[22:25], v[138:141], v[90:93], v[22:25]
	ds_read_b128 v[118:121], v161 offset:4096
	v_mfma_f32_16x16x32_f16 v[30:33], v[142:145], v[90:93], v[30:33]
	ds_read_b128 v[122:125], v161 offset:6144
	v_mfma_f32_16x16x32_f16 v[74:77], v[134:137], v[94:97], v[74:77]
	ds_read_b128 v[126:129], v161 offset:8192
	v_mfma_f32_16x16x32_f16 v[18:21], v[138:141], v[94:97], v[18:21]
	ds_read_b128 v[130:133], v161 offset:10240
	v_mfma_f32_16x16x32_f16 v[26:29], v[142:145], v[94:97], v[26:29]
	s_add_u32 m0, s11, 0x11f80
	v_mfma_f32_16x16x32_f16 v[70:73], v[134:137], v[98:101], v[70:73]
	global_load_lds_dwordx4 v[220:221], off offset:128
	v_mfma_f32_16x16x32_f16 v[46:49], v[138:141], v[98:101], v[46:49]
	v_mfma_f32_16x16x32_f16 v[240:243], v[142:145], v[98:101], v[240:243]
	s_add_u32 m0, s11, 0x13f80
	v_mfma_f32_16x16x32_f16 v[66:69], v[134:137], v[102:105], v[66:69]
	global_load_lds_dwordx4 v[224:225], off offset:128
	v_mfma_f32_16x16x32_f16 v[42:45], v[138:141], v[102:105], v[42:45]
	v_mfma_f32_16x16x32_f16 v[236:239], v[142:145], v[102:105], v[236:239]
	s_add_u32 m0, s11, 0x15f80
	v_mfma_f32_16x16x32_f16 v[62:65], v[134:137], v[106:109], v[62:65]
	global_load_lds_dwordx4 v[228:229], off offset:128
	v_mfma_f32_16x16x32_f16 v[38:41], v[138:141], v[106:109], v[38:41]
	v_mfma_f32_16x16x32_f16 v[34:37], v[142:145], v[106:109], v[34:37]
	s_waitcnt vmcnt(6) lgkmcnt(0)
	s_barrier
	ds_read_b128 v[134:137], v162
	v_mfma_f32_16x16x32_f16 v[82:85], v[146:149], v[110:113], v[82:85]
	ds_read_b128 v[138:141], v162 offset:2048
	v_mfma_f32_16x16x32_f16 v[58:61], v[150:153], v[110:113], v[58:61]
	ds_read_b128 v[142:145], v162 offset:4096
	v_mfma_f32_16x16x32_f16 v[14:17], v[154:157], v[110:113], v[14:17]
	ds_read_b128 v[86:89], v158
	v_mfma_f32_16x16x32_f16 v[78:81], v[146:149], v[114:117], v[78:81]
	ds_read_b128 v[90:93], v158 offset:2048
	v_mfma_f32_16x16x32_f16 v[22:25], v[150:153], v[114:117], v[22:25]
	ds_read_b128 v[94:97], v158 offset:4096
	v_mfma_f32_16x16x32_f16 v[30:33], v[154:157], v[114:117], v[30:33]
	ds_read_b128 v[98:101], v158 offset:6144
	v_mfma_f32_16x16x32_f16 v[74:77], v[146:149], v[118:121], v[74:77]
	ds_read_b128 v[102:105], v158 offset:8192
	v_mfma_f32_16x16x32_f16 v[18:21], v[150:153], v[118:121], v[18:21]
	ds_read_b128 v[106:109], v158 offset:10240
	v_mfma_f32_16x16x32_f16 v[26:29], v[154:157], v[118:121], v[26:29]
	s_add_u32 m0, s11, 0x17f00
	v_mfma_f32_16x16x32_f16 v[70:73], v[146:149], v[122:125], v[70:73]
	global_load_lds_dwordx4 v[218:219], off offset:256
	v_mfma_f32_16x16x32_f16 v[46:49], v[150:153], v[122:125], v[46:49]
	v_mfma_f32_16x16x32_f16 v[240:243], v[154:157], v[122:125], v[240:243]
	s_add_u32 m0, s11, 0x19f00
	v_mfma_f32_16x16x32_f16 v[66:69], v[146:149], v[126:129], v[66:69]
	global_load_lds_dwordx4 v[222:223], off offset:256
	v_mfma_f32_16x16x32_f16 v[42:45], v[150:153], v[126:129], v[42:45]
	v_mfma_f32_16x16x32_f16 v[236:239], v[154:157], v[126:129], v[236:239]
	s_add_u32 m0, s11, 0x1bf00
	v_mfma_f32_16x16x32_f16 v[62:65], v[146:149], v[130:133], v[62:65]
	global_load_lds_dwordx4 v[226:227], off offset:256
	v_mfma_f32_16x16x32_f16 v[38:41], v[150:153], v[130:133], v[38:41]
	v_mfma_f32_16x16x32_f16 v[34:37], v[154:157], v[130:133], v[34:37]
	v_lshl_add_u64 v[218:219], v[218:219], 0, s[20:21]
	v_lshl_add_u64 v[222:223], v[222:223], 0, s[20:21]
	v_lshl_add_u64 v[226:227], v[226:227], 0, s[20:21]
	v_lshl_add_u64 v[220:221], v[220:221], 0, s[20:21]
	v_lshl_add_u64 v[224:225], v[224:225], 0, s[20:21]
	v_lshl_add_u64 v[228:229], v[228:229], 0, s[20:21]
	s_sub_u32 s22, s22, 1
	s_cmp_lg_u32 s22, 0
	s_cbranch_scc1 .Lgemm_T_loop
	s_waitcnt lgkmcnt(0)
	ds_read_b128 v[146:149], v164
	v_mfma_f32_16x16x32_f16 v[82:85], v[134:137], v[86:89], v[82:85]
	ds_read_b128 v[150:153], v164 offset:2048
	v_mfma_f32_16x16x32_f16 v[58:61], v[138:141], v[86:89], v[58:61]
	ds_read_b128 v[154:157], v164 offset:4096
	v_mfma_f32_16x16x32_f16 v[14:17], v[142:145], v[86:89], v[14:17]
	ds_read_b128 v[110:113], v160
	v_mfma_f32_16x16x32_f16 v[78:81], v[134:137], v[90:93], v[78:81]
	ds_read_b128 v[114:117], v160 offset:2048
	v_mfma_f32_16x16x32_f16 v[22:25], v[138:141], v[90:93], v[22:25]
	ds_read_b128 v[118:121], v160 offset:4096
	v_mfma_f32_16x16x32_f16 v[30:33], v[142:145], v[90:93], v[30:33]
	ds_read_b128 v[122:125], v160 offset:6144
	v_mfma_f32_16x16x32_f16 v[74:77], v[134:137], v[94:97], v[74:77]
	ds_read_b128 v[126:129], v160 offset:8192
	v_mfma_f32_16x16x32_f16 v[18:21], v[138:141], v[94:97], v[18:21]
	ds_read_b128 v[130:133], v160 offset:10240
	v_mfma_f32_16x16x32_f16 v[26:29], v[142:145], v[94:97], v[26:29]
	s_add_u32 m0, s11, 0x1e080
	v_mfma_f32_16x16x32_f16 v[70:73], v[134:137], v[98:101], v[70:73]
	global_load_lds_dwordx4 v[220:221], off offset:-128
	v_mfma_f32_16x16x32_f16 v[46:49], v[138:141], v[98:101], v[46:49]
	v_mfma_f32_16x16x32_f16 v[240:243], v[142:145], v[98:101], v[240:243]
	s_add_u32 m0, s11, 0x20080
	v_mfma_f32_16x16x32_f16 v[66:69], v[134:137], v[102:105], v[66:69]
	global_load_lds_dwordx4 v[224:225], off offset:-128
	v_mfma_f32_16x16x32_f16 v[42:45], v[138:141], v[102:105], v[42:45]
	v_mfma_f32_16x16x32_f16 v[236:239], v[142:145], v[102:105], v[236:239]
	s_add_u32 m0, s11, 0x22080
	v_mfma_f32_16x16x32_f16 v[62:65], v[134:137], v[106:109], v[62:65]
	global_load_lds_dwordx4 v[228:229], off offset:-128
	v_mfma_f32_16x16x32_f16 v[38:41], v[138:141], v[106:109], v[38:41]
	v_mfma_f32_16x16x32_f16 v[34:37], v[142:145], v[106:109], v[34:37]
	s_waitcnt vmcnt(6) lgkmcnt(0)
	s_barrier
	ds_read_b128 v[134:137], v162 offset:49152
	v_mfma_f32_16x16x32_f16 v[82:85], v[146:149], v[110:113], v[82:85]
	ds_read_b128 v[138:141], v162 offset:51200
	v_mfma_f32_16x16x32_f16 v[58:61], v[150:153], v[110:113], v[58:61]
	ds_read_b128 v[142:145], v162 offset:53248
	v_mfma_f32_16x16x32_f16 v[14:17], v[154:157], v[110:113], v[14:17]
	ds_read_b128 v[86:89], v158 offset:49152
	v_mfma_f32_16x16x32_f16 v[78:81], v[146:149], v[114:117], v[78:81]
	ds_read_b128 v[90:93], v158 offset:51200
	v_mfma_f32_16x16x32_f16 v[22:25], v[150:153], v[114:117], v[22:25]
	ds_read_b128 v[94:97], v158 offset:53248
	v_mfma_f32_16x16x32_f16 v[30:33], v[154:157], v[114:117], v[30:33]
	ds_read_b128 v[98:101], v158 offset:55296
	v_mfma_f32_16x16x32_f16 v[74:77], v[146:149], v[118:121], v[74:77]
	ds_read_b128 v[102:105], v158 offset:57344
	v_mfma_f32_16x16x32_f16 v[18:21], v[150:153], v[118:121], v[18:21]
	ds_read_b128 v[106:109], v158 offset:59392
	v_mfma_f32_16x16x32_f16 v[26:29], v[154:157], v[118:121], v[26:29]
	s_add_u32 m0, s11, 0x0
	v_mfma_f32_16x16x32_f16 v[70:73], v[146:149], v[122:125], v[70:73]
	global_load_lds_dwordx4 v[218:219], off
	v_mfma_f32_16x16x32_f16 v[46:49], v[150:153], v[122:125], v[46:49]
	v_mfma_f32_16x16x32_f16 v[240:243], v[154:157], v[122:125], v[240:243]
	s_add_u32 m0, s11, 0x2000
	v_mfma_f32_16x16x32_f16 v[66:69], v[146:149], v[126:129], v[66:69]
	global_load_lds_dwordx4 v[222:223], off
	v_mfma_f32_16x16x32_f16 v[42:45], v[150:153], v[126:129], v[42:45]
	v_mfma_f32_16x16x32_f16 v[236:239], v[154:157], v[126:129], v[236:239]
	s_add_u32 m0, s11, 0x4000
	v_mfma_f32_16x16x32_f16 v[62:65], v[146:149], v[130:133], v[62:65]
	global_load_lds_dwordx4 v[226:227], off
	v_mfma_f32_16x16x32_f16 v[38:41], v[150:153], v[130:133], v[38:41]
	v_mfma_f32_16x16x32_f16 v[34:37], v[154:157], v[130:133], v[34:37]
	s_waitcnt lgkmcnt(0)
	ds_read_b128 v[146:149], v164 offset:49152
	v_mfma_f32_16x16x32_f16 v[82:85], v[134:137], v[86:89], v[82:85]
	ds_read_b128 v[150:153], v164 offset:51200
	v_mfma_f32_16x16x32_f16 v[58:61], v[138:141], v[86:89], v[58:61]
	ds_read_b128 v[154:157], v164 offset:53248
	v_mfma_f32_16x16x32_f16 v[14:17], v[142:145], v[86:89], v[14:17]
	ds_read_b128 v[110:113], v160 offset:49152
	v_mfma_f32_16x16x32_f16 v[78:81], v[134:137], v[90:93], v[78:81]
	ds_read_b128 v[114:117], v160 offset:51200
	v_mfma_f32_16x16x32_f16 v[22:25], v[138:141], v[90:93], v[22:25]
	ds_read_b128 v[118:121], v160 offset:53248
	v_mfma_f32_16x16x32_f16 v[30:33], v[142:145], v[90:93], v[30:33]
	ds_read_b128 v[122:125], v160 offset:55296
	v_mfma_f32_16x16x32_f16 v[74:77], v[134:137], v[94:97], v[74:77]
	ds_read_b128 v[126:129], v160 offset:57344
	v_mfma_f32_16x16x32_f16 v[18:21], v[138:141], v[94:97], v[18:21]
	ds_read_b128 v[130:133], v160 offset:59392
	v_mfma_f32_16x16x32_f16 v[26:29], v[142:145], v[94:97], v[26:29]
	s_add_u32 m0, s11, 0x6000
	v_mfma_f32_16x16x32_f16 v[70:73], v[134:137], v[98:101], v[70:73]
	global_load_lds_dwordx4 v[220:221], off
	v_mfma_f32_16x16x32_f16 v[46:49], v[138:141], v[98:101], v[46:49]
	v_mfma_f32_16x16x32_f16 v[240:243], v[142:145], v[98:101], v[240:243]
	s_add_u32 m0, s11, 0x8000
	v_mfma_f32_16x16x32_f16 v[66:69], v[134:137], v[102:105], v[66:69]
	global_load_lds_dwordx4 v[224:225], off
	v_mfma_f32_16x16x32_f16 v[42:45], v[138:141], v[102:105], v[42:45]
	v_mfma_f32_16x16x32_f16 v[236:239], v[142:145], v[102:105], v[236:239]
	s_add_u32 m0, s11, 0xa000
	v_mfma_f32_16x16x32_f16 v[62:65], v[134:137], v[106:109], v[62:65]
	global_load_lds_dwordx4 v[228:229], off
	v_mfma_f32_16x16x32_f16 v[38:41], v[138:141], v[106:109], v[38:41]
	v_mfma_f32_16x16x32_f16 v[34:37], v[142:145], v[106:109], v[34:37]
	s_waitcnt vmcnt(6) lgkmcnt(0)
	s_barrier
	s_lshl_b32 s26, s17, 2
	s_add_u32 s26, s24, s26
	s_addc_u32 s27, s25, 0
	v_lshlrev_b32_e32 v50, 4, v231
	global_load_dwordx4 v[10:13], v50, s[26:27]
	global_load_dwordx4 v[6:9], v50, s[26:27] offset:64
	global_load_dwordx4 v[2:5], v50, s[26:27] offset:128
	ds_read_b128 v[134:137], v163
	v_mfma_f32_16x16x32_f16 v[82:85], v[146:149], v[110:113], v[82:85]
	ds_read_b128 v[138:141], v163 offset:2048
	v_mfma_f32_16x16x32_f16 v[58:61], v[150:153], v[110:113], v[58:61]
	ds_read_b128 v[142:145], v163 offset:4096
	v_mfma_f32_16x16x32_f16 v[14:17], v[154:157], v[110:113], v[14:17]
	ds_read_b128 v[86:89], v159
	v_mfma_f32_16x16x32_f16 v[78:81], v[146:149], v[114:117], v[78:81]
	ds_read_b128 v[90:93], v159 offset:2048
	v_mfma_f32_16x16x32_f16 v[22:25], v[150:153], v[114:117], v[22:25]
	ds_read_b128 v[94:97], v159 offset:4096
	v_mfma_f32_16x16x32_f16 v[30:33], v[154:157], v[114:117], v[30:33]
	ds_read_b128 v[98:101], v159 offset:6144
	v_mfma_f32_16x16x32_f16 v[74:77], v[146:149], v[118:121], v[74:77]
	ds_read_b128 v[102:105], v159 offset:8192
	v_mfma_f32_16x16x32_f16 v[18:21], v[150:153], v[118:121], v[18:21]
	ds_read_b128 v[106:109], v159 offset:10240
	v_mfma_f32_16x16x32_f16 v[26:29], v[154:157], v[118:121], v[26:29]
	v_mfma_f32_16x16x32_f16 v[70:73], v[146:149], v[122:125], v[70:73]
	v_mfma_f32_16x16x32_f16 v[46:49], v[150:153], v[122:125], v[46:49]
	v_mfma_f32_16x16x32_f16 v[240:243], v[154:157], v[122:125], v[240:243]
	v_mfma_f32_16x16x32_f16 v[66:69], v[146:149], v[126:129], v[66:69]
	v_mfma_f32_16x16x32_f16 v[42:45], v[150:153], v[126:129], v[42:45]
	v_mfma_f32_16x16x32_f16 v[236:239], v[154:157], v[126:129], v[236:239]
	v_mfma_f32_16x16x32_f16 v[62:65], v[146:149], v[130:133], v[62:65]
	v_mfma_f32_16x16x32_f16 v[38:41], v[150:153], v[130:133], v[38:41]
	v_mfma_f32_16x16x32_f16 v[34:37], v[154:157], v[130:133], v[34:37]
	s_waitcnt lgkmcnt(0)
	ds_read_b128 v[146:149], v165
	v_mfma_f32_16x16x32_f16 v[82:85], v[134:137], v[86:89], v[82:85]
	ds_read_b128 v[150:153], v165 offset:2048
	v_mfma_f32_16x16x32_f16 v[58:61], v[138:141], v[86:89], v[58:61]
	ds_read_b128 v[154:157], v165 offset:4096
	v_mfma_f32_16x16x32_f16 v[14:17], v[142:145], v[86:89], v[14:17]
	ds_read_b128 v[110:113], v161
	v_mfma_f32_16x16x32_f16 v[78:81], v[134:137], v[90:93], v[78:81]
	ds_read_b128 v[114:117], v161 offset:2048
	v_mfma_f32_16x16x32_f16 v[22:25], v[138:141], v[90:93], v[22:25]
	ds_read_b128 v[118:121], v161 offset:4096
	v_mfma_f32_16x16x32_f16 v[30:33], v[142:145], v[90:93], v[30:33]
	ds_read_b128 v[122:125], v161 offset:6144
	v_mfma_f32_16x16x32_f16 v[74:77], v[134:137], v[94:97], v[74:77]
	ds_read_b128 v[126:129], v161 offset:8192
	v_mfma_f32_16x16x32_f16 v[18:21], v[138:141], v[94:97], v[18:21]
	ds_read_b128 v[130:133], v161 offset:10240
	v_mfma_f32_16x16x32_f16 v[26:29], v[142:145], v[94:97], v[26:29]
	v_mfma_f32_16x16x32_f16 v[70:73], v[134:137], v[98:101], v[70:73]
	v_mfma_f32_16x16x32_f16 v[46:49], v[138:141], v[98:101], v[46:49]
	v_mfma_f32_16x16x32_f16 v[240:243], v[142:145], v[98:101], v[240:243]
	v_mfma_f32_16x16x32_f16 v[66:69], v[134:137], v[102:105], v[66:69]
	v_mfma_f32_16x16x32_f16 v[42:45], v[138:141], v[102:105], v[42:45]
	v_mfma_f32_16x16x32_f16 v[236:239], v[142:145], v[102:105], v[236:239]
	v_mfma_f32_16x16x32_f16 v[62:65], v[134:137], v[106:109], v[62:65]
	v_mfma_f32_16x16x32_f16 v[38:41], v[138:141], v[106:109], v[38:41]
	v_mfma_f32_16x16x32_f16 v[34:37], v[142:145], v[106:109], v[34:37]
	s_waitcnt vmcnt(3) lgkmcnt(0)
	s_barrier
	ds_read_b128 v[134:137], v162
	v_mfma_f32_16x16x32_f16 v[82:85], v[146:149], v[110:113], v[82:85]
	ds_read_b128 v[138:141], v162 offset:2048
	v_mfma_f32_16x16x32_f16 v[58:61], v[150:153], v[110:113], v[58:61]
	ds_read_b128 v[142:145], v162 offset:4096
	v_mfma_f32_16x16x32_f16 v[14:17], v[154:157], v[110:113], v[14:17]
	ds_read_b128 v[86:89], v158
	v_mfma_f32_16x16x32_f16 v[78:81], v[146:149], v[114:117], v[78:81]
	ds_read_b128 v[90:93], v158 offset:2048
	v_mfma_f32_16x16x32_f16 v[22:25], v[150:153], v[114:117], v[22:25]
	ds_read_b128 v[94:97], v158 offset:4096
	v_mfma_f32_16x16x32_f16 v[30:33], v[154:157], v[114:117], v[30:33]
	ds_read_b128 v[98:101], v158 offset:6144
	v_mfma_f32_16x16x32_f16 v[74:77], v[146:149], v[118:121], v[74:77]
	ds_read_b128 v[102:105], v158 offset:8192
	v_mfma_f32_16x16x32_f16 v[18:21], v[150:153], v[118:121], v[18:21]
	ds_read_b128 v[106:109], v158 offset:10240
	v_mfma_f32_16x16x32_f16 v[26:29], v[154:157], v[118:121], v[26:29]
	v_mfma_f32_16x16x32_f16 v[70:73], v[146:149], v[122:125], v[70:73]
	v_mfma_f32_16x16x32_f16 v[46:49], v[150:153], v[122:125], v[46:49]
	v_mfma_f32_16x16x32_f16 v[240:243], v[154:157], v[122:125], v[240:243]
	v_mfma_f32_16x16x32_f16 v[66:69], v[146:149], v[126:129], v[66:69]
	v_mfma_f32_16x16x32_f16 v[42:45], v[150:153], v[126:129], v[42:45]
	v_mfma_f32_16x16x32_f16 v[236:239], v[154:157], v[126:129], v[236:239]
	v_mfma_f32_16x16x32_f16 v[62:65], v[146:149], v[130:133], v[62:65]
	v_mfma_f32_16x16x32_f16 v[38:41], v[150:153], v[130:133], v[38:41]
	v_mfma_f32_16x16x32_f16 v[34:37], v[154:157], v[130:133], v[34:37]
	s_waitcnt lgkmcnt(0)
	ds_read_b128 v[146:149], v164
	v_mfma_f32_16x16x32_f16 v[82:85], v[134:137], v[86:89], v[82:85]
	ds_read_b128 v[150:153], v164 offset:2048
	v_mfma_f32_16x16x32_f16 v[58:61], v[138:141], v[86:89], v[58:61]
	ds_read_b128 v[154:157], v164 offset:4096
	v_mfma_f32_16x16x32_f16 v[14:17], v[142:145], v[86:89], v[14:17]
	ds_read_b128 v[110:113], v160
	v_mfma_f32_16x16x32_f16 v[78:81], v[134:137], v[90:93], v[78:81]
	ds_read_b128 v[114:117], v160 offset:2048
	v_mfma_f32_16x16x32_f16 v[22:25], v[138:141], v[90:93], v[22:25]
	ds_read_b128 v[118:121], v160 offset:4096
	v_mfma_f32_16x16x32_f16 v[30:33], v[142:145], v[90:93], v[30:33]
	ds_read_b128 v[122:125], v160 offset:6144
	v_mfma_f32_16x16x32_f16 v[74:77], v[134:137], v[94:97], v[74:77]
	ds_read_b128 v[126:129], v160 offset:8192
	v_mfma_f32_16x16x32_f16 v[18:21], v[138:141], v[94:97], v[18:21]
	ds_read_b128 v[130:133], v160 offset:10240
	v_mfma_f32_16x16x32_f16 v[26:29], v[142:145], v[94:97], v[26:29]
	v_mfma_f32_16x16x32_f16 v[70:73], v[134:137], v[98:101], v[70:73]
	v_mfma_f32_16x16x32_f16 v[46:49], v[138:141], v[98:101], v[46:49]
	v_mfma_f32_16x16x32_f16 v[240:243], v[142:145], v[98:101], v[240:243]
	v_mfma_f32_16x16x32_f16 v[66:69], v[134:137], v[102:105], v[66:69]
	v_mfma_f32_16x16x32_f16 v[42:45], v[138:141], v[102:105], v[42:45]
	v_mfma_f32_16x16x32_f16 v[236:239], v[142:145], v[102:105], v[236:239]
	v_mfma_f32_16x16x32_f16 v[62:65], v[134:137], v[106:109], v[62:65]
	v_mfma_f32_16x16x32_f16 v[38:41], v[138:141], v[106:109], v[38:41]
	v_mfma_f32_16x16x32_f16 v[34:37], v[142:145], v[106:109], v[34:37]
	s_waitcnt lgkmcnt(0)
	v_mfma_f32_16x16x32_f16 v[82:85], v[146:149], v[110:113], v[82:85]
	v_mfma_f32_16x16x32_f16 v[58:61], v[150:153], v[110:113], v[58:61]
	v_mfma_f32_16x16x32_f16 v[14:17], v[154:157], v[110:113], v[14:17]
	v_mfma_f32_16x16x32_f16 v[78:81], v[146:149], v[114:117], v[78:81]
	v_mfma_f32_16x16x32_f16 v[22:25], v[150:153], v[114:117], v[22:25]
	v_mfma_f32_16x16x32_f16 v[30:33], v[154:157], v[114:117], v[30:33]
	v_mfma_f32_16x16x32_f16 v[74:77], v[146:149], v[118:121], v[74:77]
	v_mfma_f32_16x16x32_f16 v[18:21], v[150:153], v[118:121], v[18:21]
	v_mfma_f32_16x16x32_f16 v[26:29], v[154:157], v[118:121], v[26:29]
	v_mfma_f32_16x16x32_f16 v[70:73], v[146:149], v[122:125], v[70:73]
	v_mfma_f32_16x16x32_f16 v[46:49], v[150:153], v[122:125], v[46:49]
	v_mfma_f32_16x16x32_f16 v[240:243], v[154:157], v[122:125], v[240:243]
	v_mfma_f32_16x16x32_f16 v[66:69], v[146:149], v[126:129], v[66:69]
	v_mfma_f32_16x16x32_f16 v[42:45], v[150:153], v[126:129], v[42:45]
	v_mfma_f32_16x16x32_f16 v[236:239], v[154:157], v[126:129], v[236:239]
	v_mfma_f32_16x16x32_f16 v[62:65], v[146:149], v[130:133], v[62:65]
	v_mfma_f32_16x16x32_f16 v[38:41], v[150:153], v[130:133], v[38:41]
	v_mfma_f32_16x16x32_f16 v[34:37], v[154:157], v[130:133], v[34:37]
	s_branch .LBB1_76
.Lgemm_N_loop:
	s_waitcnt lgkmcnt(0)
	ds_read_b128 v[146:149], v164
	v_mfma_f32_16x16x32_f16 v[82:85], v[86:89], v[134:137], v[82:85]
	ds_read_b128 v[150:153], v164 offset:2048
	v_mfma_f32_16x16x32_f16 v[58:61], v[86:89], v[138:141], v[58:61]
	ds_read_b128 v[154:157], v164 offset:4096
	v_mfma_f32_16x16x32_f16 v[14:17], v[86:89], v[142:145], v[14:17]
	ds_read_b128 v[110:113], v160
	v_mfma_f32_16x16x32_f16 v[78:81], v[90:93], v[134:137], v[78:81]
	ds_read_b128 v[114:117], v160 offset:2048
	v_mfma_f32_16x16x32_f16 v[22:25], v[90:93], v[138:141], v[22:25]
	ds_read_b128 v[118:121], v160 offset:4096
	v_mfma_f32_16x16x32_f16 v[30:33], v[90:93], v[142:145], v[30:33]
	ds_read_b128 v[122:125], v160 offset:6144
	v_mfma_f32_16x16x32_f16 v[74:77], v[94:97], v[134:137], v[74:77]
	ds_read_b128 v[126:129], v160 offset:8192
	v_mfma_f32_16x16x32_f16 v[18:21], v[94:97], v[138:141], v[18:21]
	ds_read_b128 v[130:133], v160 offset:10240
	v_mfma_f32_16x16x32_f16 v[26:29], v[94:97], v[142:145], v[26:29]
	s_add_u32 m0, s11, 0x1e080
	v_mfma_f32_16x16x32_f16 v[70:73], v[98:101], v[134:137], v[70:73]
	global_load_lds_dwordx4 v[220:221], off offset:-128
	v_mfma_f32_16x16x32_f16 v[46:49], v[98:101], v[138:141], v[46:49]
	v_mfma_f32_16x16x32_f16 v[240:243], v[98:101], v[142:145], v[240:243]
	s_add_u32 m0, s11, 0x20080
	v_mfma_f32_16x16x32_f16 v[66:69], v[102:105], v[134:137], v[66:69]
	global_load_lds_dwordx4 v[224:225], off offset:-128
	v_mfma_f32_16x16x32_f16 v[42:45], v[102:105], v[138:141], v[42:45]
	v_mfma_f32_16x16x32_f16 v[236:239], v[102:105], v[142:145], v[236:239]
	s_add_u32 m0, s11, 0x22080
	v_mfma_f32_16x16x32_f16 v[62:65], v[106:109], v[134:137], v[62:65]
	global_load_lds_dwordx4 v[228:229], off offset:-128
	v_mfma_f32_16x16x32_f16 v[38:41], v[106:109], v[138:141], v[38:41]
	v_mfma_f32_16x16x32_f16 v[34:37], v[106:109], v[142:145], v[34:37]
	s_waitcnt vmcnt(6) lgkmcnt(0)
	s_barrier
	ds_read_b128 v[134:137], v162 offset:49152
	v_mfma_f32_16x16x32_f16 v[82:85], v[110:113], v[146:149], v[82:85]
	ds_read_b128 v[138:141], v162 offset:51200
	v_mfma_f32_16x16x32_f16 v[58:61], v[110:113], v[150:153], v[58:61]
	ds_read_b128 v[142:145], v162 offset:53248
	v_mfma_f32_16x16x32_f16 v[14:17], v[110:113], v[154:157], v[14:17]
	ds_read_b128 v[86:89], v158 offset:49152
	v_mfma_f32_16x16x32_f16 v[78:81], v[114:117], v[146:149], v[78:81]
	ds_read_b128 v[90:93], v158 offset:51200
	v_mfma_f32_16x16x32_f16 v[22:25], v[114:117], v[150:153], v[22:25]
	ds_read_b128 v[94:97], v158 offset:53248
	v_mfma_f32_16x16x32_f16 v[30:33], v[114:117], v[154:157], v[30:33]
	ds_read_b128 v[98:101], v158 offset:55296
	v_mfma_f32_16x16x32_f16 v[74:77], v[118:121], v[146:149], v[74:77]
	ds_read_b128 v[102:105], v158 offset:57344
	v_mfma_f32_16x16x32_f16 v[18:21], v[118:121], v[150:153], v[18:21]
	ds_read_b128 v[106:109], v158 offset:59392
	v_mfma_f32_16x16x32_f16 v[26:29], v[118:121], v[154:157], v[26:29]
	s_add_u32 m0, s11, 0x0
	v_mfma_f32_16x16x32_f16 v[70:73], v[122:125], v[146:149], v[70:73]
	global_load_lds_dwordx4 v[218:219], off
	v_mfma_f32_16x16x32_f16 v[46:49], v[122:125], v[150:153], v[46:49]
	v_mfma_f32_16x16x32_f16 v[240:243], v[122:125], v[154:157], v[240:243]
	s_add_u32 m0, s11, 0x2000
	v_mfma_f32_16x16x32_f16 v[66:69], v[126:129], v[146:149], v[66:69]
	global_load_lds_dwordx4 v[222:223], off
	v_mfma_f32_16x16x32_f16 v[42:45], v[126:129], v[150:153], v[42:45]
	v_mfma_f32_16x16x32_f16 v[236:239], v[126:129], v[154:157], v[236:239]
	s_add_u32 m0, s11, 0x4000
	v_mfma_f32_16x16x32_f16 v[62:65], v[130:133], v[146:149], v[62:65]
	global_load_lds_dwordx4 v[226:227], off
	v_mfma_f32_16x16x32_f16 v[38:41], v[130:133], v[150:153], v[38:41]
	v_mfma_f32_16x16x32_f16 v[34:37], v[130:133], v[154:157], v[34:37]
	s_waitcnt lgkmcnt(0)
	ds_read_b128 v[146:149], v164 offset:49152
	v_mfma_f32_16x16x32_f16 v[82:85], v[86:89], v[134:137], v[82:85]
	ds_read_b128 v[150:153], v164 offset:51200
	v_mfma_f32_16x16x32_f16 v[58:61], v[86:89], v[138:141], v[58:61]
	ds_read_b128 v[154:157], v164 offset:53248
	v_mfma_f32_16x16x32_f16 v[14:17], v[86:89], v[142:145], v[14:17]
	ds_read_b128 v[110:113], v160 offset:49152
	v_mfma_f32_16x16x32_f16 v[78:81], v[90:93], v[134:137], v[78:81]
	ds_read_b128 v[114:117], v160 offset:51200
	v_mfma_f32_16x16x32_f16 v[22:25], v[90:93], v[138:141], v[22:25]
	ds_read_b128 v[118:121], v160 offset:53248
	v_mfma_f32_16x16x32_f16 v[30:33], v[90:93], v[142:145], v[30:33]
	ds_read_b128 v[122:125], v160 offset:55296
	v_mfma_f32_16x16x32_f16 v[74:77], v[94:97], v[134:137], v[74:77]
	ds_read_b128 v[126:129], v160 offset:57344
	v_mfma_f32_16x16x32_f16 v[18:21], v[94:97], v[138:141], v[18:21]
	ds_read_b128 v[130:133], v160 offset:59392
	v_mfma_f32_16x16x32_f16 v[26:29], v[94:97], v[142:145], v[26:29]
	s_add_u32 m0, s11, 0x6000
	v_mfma_f32_16x16x32_f16 v[70:73], v[98:101], v[134:137], v[70:73]
	global_load_lds_dwordx4 v[220:221], off
	v_mfma_f32_16x16x32_f16 v[46:49], v[98:101], v[138:141], v[46:49]
	v_mfma_f32_16x16x32_f16 v[240:243], v[98:101], v[142:145], v[240:243]
	s_add_u32 m0, s11, 0x8000
	v_mfma_f32_16x16x32_f16 v[66:69], v[102:105], v[134:137], v[66:69]
	global_load_lds_dwordx4 v[224:225], off
	v_mfma_f32_16x16x32_f16 v[42:45], v[102:105], v[138:141], v[42:45]
	v_mfma_f32_16x16x32_f16 v[236:239], v[102:105], v[142:145], v[236:239]
	s_add_u32 m0, s11, 0xa000
	v_mfma_f32_16x16x32_f16 v[62:65], v[106:109], v[134:137], v[62:65]
	global_load_lds_dwordx4 v[228:229], off
	v_mfma_f32_16x16x32_f16 v[38:41], v[106:109], v[138:141], v[38:41]
	v_mfma_f32_16x16x32_f16 v[34:37], v[106:109], v[142:145], v[34:37]
	s_waitcnt vmcnt(6) lgkmcnt(0)
	s_barrier
	ds_read_b128 v[134:137], v163
	v_mfma_f32_16x16x32_f16 v[82:85], v[110:113], v[146:149], v[82:85]
	ds_read_b128 v[138:141], v163 offset:2048
	v_mfma_f32_16x16x32_f16 v[58:61], v[110:113], v[150:153], v[58:61]
	ds_read_b128 v[142:145], v163 offset:4096
	v_mfma_f32_16x16x32_f16 v[14:17], v[110:113], v[154:157], v[14:17]
	ds_read_b128 v[86:89], v159
	v_mfma_f32_16x16x32_f16 v[78:81], v[114:117], v[146:149], v[78:81]
	ds_read_b128 v[90:93], v159 offset:2048
	v_mfma_f32_16x16x32_f16 v[22:25], v[114:117], v[150:153], v[22:25]
	ds_read_b128 v[94:97], v159 offset:4096
	v_mfma_f32_16x16x32_f16 v[30:33], v[114:117], v[154:157], v[30:33]
	ds_read_b128 v[98:101], v159 offset:6144
	v_mfma_f32_16x16x32_f16 v[74:77], v[118:121], v[146:149], v[74:77]
	ds_read_b128 v[102:105], v159 offset:8192
	v_mfma_f32_16x16x32_f16 v[18:21], v[118:121], v[150:153], v[18:21]
	ds_read_b128 v[106:109], v159 offset:10240
	v_mfma_f32_16x16x32_f16 v[26:29], v[118:121], v[154:157], v[26:29]
	s_add_u32 m0, s11, 0xbf80
	v_mfma_f32_16x16x32_f16 v[70:73], v[122:125], v[146:149], v[70:73]
	global_load_lds_dwordx4 v[218:219], off offset:128
	v_mfma_f32_16x16x32_f16 v[46:49], v[122:125], v[150:153], v[46:49]
	v_mfma_f32_16x16x32_f16 v[240:243], v[122:125], v[154:157], v[240:243]
	s_add_u32 m0, s11, 0xdf80
	v_mfma_f32_16x16x32_f16 v[66:69], v[126:129], v[146:149], v[66:69]
	global_load_lds_dwordx4 v[222:223], off offset:128
	v_mfma_f32_16x16x32_f16 v[42:45], v[126:129], v[150:153], v[42:45]
	v_mfma_f32_16x16x32_f16 v[236:239], v[126:129], v[154:157], v[236:239]
	s_add_u32 m0, s11, 0xff80
	v_mfma_f32_16x16x32_f16 v[62:65], v[130:133], v[146:149], v[62:65]
	global_load_lds_dwordx4 v[226:227], off offset:128
	v_mfma_f32_16x16x32_f16 v[38:41], v[130:133], v[150:153], v[38:41]
	v_mfma_f32_16x16x32_f16 v[34:37], v[130:133], v[154:157], v[34:37]
	s_waitcnt lgkmcnt(0)
	ds_read_b128 v[146:149], v165
	v_mfma_f32_16x16x32_f16 v[82:85], v[86:89], v[134:137], v[82:85]
	ds_read_b128 v[150:153], v165 offset:2048
	v_mfma_f32_16x16x32_f16 v[58:61], v[86:89], v[138:141], v[58:61]
	ds_read_b128 v[154:157], v165 offset:4096
	v_mfma_f32_16x16x32_f16 v[14:17], v[86:89], v[142:145], v[14:17]
	ds_read_b128 v[110:113], v161
	v_mfma_f32_16x16x32_f16 v[78:81], v[90:93], v[134:137], v[78:81]
	ds_read_b128 v[114:117], v161 offset:2048
	v_mfma_f32_16x16x32_f16 v[22:25], v[90:93], v[138:141], v[22:25]
	ds_read_b128 v[118:121], v161 offset:4096
	v_mfma_f32_16x16x32_f16 v[30:33], v[90:93], v[142:145], v[30:33]
	ds_read_b128 v[122:125], v161 offset:6144
	v_mfma_f32_16x16x32_f16 v[74:77], v[94:97], v[134:137], v[74:77]
	ds_read_b128 v[126:129], v161 offset:8192
	v_mfma_f32_16x16x32_f16 v[18:21], v[94:97], v[138:141], v[18:21]
	ds_read_b128 v[130:133], v161 offset:10240
	v_mfma_f32_16x16x32_f16 v[26:29], v[94:97], v[142:145], v[26:29]
	s_add_u32 m0, s11, 0x11f80
	v_mfma_f32_16x16x32_f16 v[70:73], v[98:101], v[134:137], v[70:73]
	global_load_lds_dwordx4 v[220:221], off offset:128
	v_mfma_f32_16x16x32_f16 v[46:49], v[98:101], v[138:141], v[46:49]
	v_mfma_f32_16x16x32_f16 v[240:243], v[98:101], v[142:145], v[240:243]
	s_add_u32 m0, s11, 0x13f80
	v_mfma_f32_16x16x32_f16 v[66:69], v[102:105], v[134:137], v[66:69]
	global_load_lds_dwordx4 v[224:225], off offset:128
	v_mfma_f32_16x16x32_f16 v[42:45], v[102:105], v[138:141], v[42:45]
	v_mfma_f32_16x16x32_f16 v[236:239], v[102:105], v[142:145], v[236:239]
	s_add_u32 m0, s11, 0x15f80
	v_mfma_f32_16x16x32_f16 v[62:65], v[106:109], v[134:137], v[62:65]
	global_load_lds_dwordx4 v[228:229], off offset:128
	v_mfma_f32_16x16x32_f16 v[38:41], v[106:109], v[138:141], v[38:41]
	v_mfma_f32_16x16x32_f16 v[34:37], v[106:109], v[142:145], v[34:37]
	s_waitcnt vmcnt(6) lgkmcnt(0)
	s_barrier
	ds_read_b128 v[134:137], v162
	v_mfma_f32_16x16x32_f16 v[82:85], v[110:113], v[146:149], v[82:85]
	ds_read_b128 v[138:141], v162 offset:2048
	v_mfma_f32_16x16x32_f16 v[58:61], v[110:113], v[150:153], v[58:61]
	ds_read_b128 v[142:145], v162 offset:4096
	v_mfma_f32_16x16x32_f16 v[14:17], v[110:113], v[154:157], v[14:17]
	ds_read_b128 v[86:89], v158
	v_mfma_f32_16x16x32_f16 v[78:81], v[114:117], v[146:149], v[78:81]
	ds_read_b128 v[90:93], v158 offset:2048
	v_mfma_f32_16x16x32_f16 v[22:25], v[114:117], v[150:153], v[22:25]
	ds_read_b128 v[94:97], v158 offset:4096
	v_mfma_f32_16x16x32_f16 v[30:33], v[114:117], v[154:157], v[30:33]
	ds_read_b128 v[98:101], v158 offset:6144
	v_mfma_f32_16x16x32_f16 v[74:77], v[118:121], v[146:149], v[74:77]
	ds_read_b128 v[102:105], v158 offset:8192
	v_mfma_f32_16x16x32_f16 v[18:21], v[118:121], v[150:153], v[18:21]
	ds_read_b128 v[106:109], v158 offset:10240
	v_mfma_f32_16x16x32_f16 v[26:29], v[118:121], v[154:157], v[26:29]
	s_add_u32 m0, s11, 0x17f00
	v_mfma_f32_16x16x32_f16 v[70:73], v[122:125], v[146:149], v[70:73]
	global_load_lds_dwordx4 v[218:219], off offset:256
	v_mfma_f32_16x16x32_f16 v[46:49], v[122:125], v[150:153], v[46:49]
	v_mfma_f32_16x16x32_f16 v[240:243], v[122:125], v[154:157], v[240:243]
	s_add_u32 m0, s11, 0x19f00
	v_mfma_f32_16x16x32_f16 v[66:69], v[126:129], v[146:149], v[66:69]
	global_load_lds_dwordx4 v[222:223], off offset:256
	v_mfma_f32_16x16x32_f16 v[42:45], v[126:129], v[150:153], v[42:45]
	v_mfma_f32_16x16x32_f16 v[236:239], v[126:129], v[154:157], v[236:239]
	s_add_u32 m0, s11, 0x1bf00
	v_mfma_f32_16x16x32_f16 v[62:65], v[130:133], v[146:149], v[62:65]
	global_load_lds_dwordx4 v[226:227], off offset:256
	v_mfma_f32_16x16x32_f16 v[38:41], v[130:133], v[150:153], v[38:41]
	v_mfma_f32_16x16x32_f16 v[34:37], v[130:133], v[154:157], v[34:37]
	v_lshl_add_u64 v[218:219], v[218:219], 0, s[20:21]
	v_lshl_add_u64 v[222:223], v[222:223], 0, s[20:21]
	v_lshl_add_u64 v[226:227], v[226:227], 0, s[20:21]
	v_lshl_add_u64 v[220:221], v[220:221], 0, s[20:21]
	v_lshl_add_u64 v[224:225], v[224:225], 0, s[20:21]
	v_lshl_add_u64 v[228:229], v[228:229], 0, s[20:21]
	s_sub_u32 s22, s22, 1
	s_cmp_lg_u32 s22, 0
	s_cbranch_scc1 .Lgemm_N_loop
	s_waitcnt lgkmcnt(0)
	ds_read_b128 v[146:149], v164
	v_mfma_f32_16x16x32_f16 v[82:85], v[86:89], v[134:137], v[82:85]
	ds_read_b128 v[150:153], v164 offset:2048
	v_mfma_f32_16x16x32_f16 v[58:61], v[86:89], v[138:141], v[58:61]
	ds_read_b128 v[154:157], v164 offset:4096
	v_mfma_f32_16x16x32_f16 v[14:17], v[86:89], v[142:145], v[14:17]
	ds_read_b128 v[110:113], v160
	v_mfma_f32_16x16x32_f16 v[78:81], v[90:93], v[134:137], v[78:81]
	ds_read_b128 v[114:117], v160 offset:2048
	v_mfma_f32_16x16x32_f16 v[22:25], v[90:93], v[138:141], v[22:25]
	ds_read_b128 v[118:121], v160 offset:4096
	v_mfma_f32_16x16x32_f16 v[30:33], v[90:93], v[142:145], v[30:33]
	ds_read_b128 v[122:125], v160 offset:6144
	v_mfma_f32_16x16x32_f16 v[74:77], v[94:97], v[134:137], v[74:77]
	ds_read_b128 v[126:129], v160 offset:8192
	v_mfma_f32_16x16x32_f16 v[18:21], v[94:97], v[138:141], v[18:21]
	ds_read_b128 v[130:133], v160 offset:10240
	v_mfma_f32_16x16x32_f16 v[26:29], v[94:97], v[142:145], v[26:29]
	s_add_u32 m0, s11, 0x1e080
	v_mfma_f32_16x16x32_f16 v[70:73], v[98:101], v[134:137], v[70:73]
	global_load_lds_dwordx4 v[220:221], off offset:-128
	v_mfma_f32_16x16x32_f16 v[46:49], v[98:101], v[138:141], v[46:49]
	v_mfma_f32_16x16x32_f16 v[240:243], v[98:101], v[142:145], v[240:243]
	s_add_u32 m0, s11, 0x20080
	v_mfma_f32_16x16x32_f16 v[66:69], v[102:105], v[134:137], v[66:69]
	global_load_lds_dwordx4 v[224:225], off offset:-128
	v_mfma_f32_16x16x32_f16 v[42:45], v[102:105], v[138:141], v[42:45]
	v_mfma_f32_16x16x32_f16 v[236:239], v[102:105], v[142:145], v[236:239]
	s_add_u32 m0, s11, 0x22080
	v_mfma_f32_16x16x32_f16 v[62:65], v[106:109], v[134:137], v[62:65]
	global_load_lds_dwordx4 v[228:229], off offset:-128
	v_mfma_f32_16x16x32_f16 v[38:41], v[106:109], v[138:141], v[38:41]
	v_mfma_f32_16x16x32_f16 v[34:37], v[106:109], v[142:145], v[34:37]
	s_waitcnt vmcnt(6) lgkmcnt(0)
	s_barrier
	ds_read_b128 v[134:137], v162 offset:49152
	v_mfma_f32_16x16x32_f16 v[82:85], v[110:113], v[146:149], v[82:85]
	ds_read_b128 v[138:141], v162 offset:51200
	v_mfma_f32_16x16x32_f16 v[58:61], v[110:113], v[150:153], v[58:61]
	ds_read_b128 v[142:145], v162 offset:53248
	v_mfma_f32_16x16x32_f16 v[14:17], v[110:113], v[154:157], v[14:17]
	ds_read_b128 v[86:89], v158 offset:49152
	v_mfma_f32_16x16x32_f16 v[78:81], v[114:117], v[146:149], v[78:81]
	ds_read_b128 v[90:93], v158 offset:51200
	v_mfma_f32_16x16x32_f16 v[22:25], v[114:117], v[150:153], v[22:25]
	ds_read_b128 v[94:97], v158 offset:53248
	v_mfma_f32_16x16x32_f16 v[30:33], v[114:117], v[154:157], v[30:33]
	ds_read_b128 v[98:101], v158 offset:55296
	v_mfma_f32_16x16x32_f16 v[74:77], v[118:121], v[146:149], v[74:77]
	ds_read_b128 v[102:105], v158 offset:57344
	v_mfma_f32_16x16x32_f16 v[18:21], v[118:121], v[150:153], v[18:21]
	ds_read_b128 v[106:109], v158 offset:59392
	v_mfma_f32_16x16x32_f16 v[26:29], v[118:121], v[154:157], v[26:29]
	s_add_u32 m0, s11, 0x0
	v_mfma_f32_16x16x32_f16 v[70:73], v[122:125], v[146:149], v[70:73]
	global_load_lds_dwordx4 v[218:219], off
	v_mfma_f32_16x16x32_f16 v[46:49], v[122:125], v[150:153], v[46:49]
	v_mfma_f32_16x16x32_f16 v[240:243], v[122:125], v[154:157], v[240:243]
	s_add_u32 m0, s11, 0x2000
	v_mfma_f32_16x16x32_f16 v[66:69], v[126:129], v[146:149], v[66:69]
	global_load_lds_dwordx4 v[222:223], off
	v_mfma_f32_16x16x32_f16 v[42:45], v[126:129], v[150:153], v[42:45]
	v_mfma_f32_16x16x32_f16 v[236:239], v[126:129], v[154:157], v[236:239]
	s_add_u32 m0, s11, 0x4000
	v_mfma_f32_16x16x32_f16 v[62:65], v[130:133], v[146:149], v[62:65]
	global_load_lds_dwordx4 v[226:227], off
	v_mfma_f32_16x16x32_f16 v[38:41], v[130:133], v[150:153], v[38:41]
	v_mfma_f32_16x16x32_f16 v[34:37], v[130:133], v[154:157], v[34:37]
	s_waitcnt lgkmcnt(0)
	ds_read_b128 v[146:149], v164 offset:49152
	v_mfma_f32_16x16x32_f16 v[82:85], v[86:89], v[134:137], v[82:85]
	ds_read_b128 v[150:153], v164 offset:51200
	v_mfma_f32_16x16x32_f16 v[58:61], v[86:89], v[138:141], v[58:61]
	ds_read_b128 v[154:157], v164 offset:53248
	v_mfma_f32_16x16x32_f16 v[14:17], v[86:89], v[142:145], v[14:17]
	ds_read_b128 v[110:113], v160 offset:49152
	v_mfma_f32_16x16x32_f16 v[78:81], v[90:93], v[134:137], v[78:81]
	ds_read_b128 v[114:117], v160 offset:51200
	v_mfma_f32_16x16x32_f16 v[22:25], v[90:93], v[138:141], v[22:25]
	ds_read_b128 v[118:121], v160 offset:53248
	v_mfma_f32_16x16x32_f16 v[30:33], v[90:93], v[142:145], v[30:33]
	ds_read_b128 v[122:125], v160 offset:55296
	v_mfma_f32_16x16x32_f16 v[74:77], v[94:97], v[134:137], v[74:77]
	ds_read_b128 v[126:129], v160 offset:57344
	v_mfma_f32_16x16x32_f16 v[18:21], v[94:97], v[138:141], v[18:21]
	ds_read_b128 v[130:133], v160 offset:59392
	v_mfma_f32_16x16x32_f16 v[26:29], v[94:97], v[142:145], v[26:29]
	s_add_u32 m0, s11, 0x6000
	v_mfma_f32_16x16x32_f16 v[70:73], v[98:101], v[134:137], v[70:73]
	global_load_lds_dwordx4 v[220:221], off
	v_mfma_f32_16x16x32_f16 v[46:49], v[98:101], v[138:141], v[46:49]
	v_mfma_f32_16x16x32_f16 v[240:243], v[98:101], v[142:145], v[240:243]
	s_add_u32 m0, s11, 0x8000
	v_mfma_f32_16x16x32_f16 v[66:69], v[102:105], v[134:137], v[66:69]
	global_load_lds_dwordx4 v[224:225], off
	v_mfma_f32_16x16x32_f16 v[42:45], v[102:105], v[138:141], v[42:45]
	v_mfma_f32_16x16x32_f16 v[236:239], v[102:105], v[142:145], v[236:239]
	s_add_u32 m0, s11, 0xa000
	v_mfma_f32_16x16x32_f16 v[62:65], v[106:109], v[134:137], v[62:65]
	global_load_lds_dwordx4 v[228:229], off
	v_mfma_f32_16x16x32_f16 v[38:41], v[106:109], v[138:141], v[38:41]
	v_mfma_f32_16x16x32_f16 v[34:37], v[106:109], v[142:145], v[34:37]
	s_waitcnt vmcnt(6) lgkmcnt(0)
	s_barrier
	s_lshl_b32 s26, s17, 2
	s_add_u32 s26, s24, s26
	s_addc_u32 s27, s25, 0
	v_lshlrev_b32_e32 v50, 2, v1
	global_load_dword v234, v50, s[26:27]
	global_load_dword v232, v50, s[26:27] offset:64
	global_load_dword v230, v50, s[26:27] offset:128
	ds_read_b128 v[134:137], v163
	v_mfma_f32_16x16x32_f16 v[82:85], v[110:113], v[146:149], v[82:85]
	ds_read_b128 v[138:141], v163 offset:2048
	v_mfma_f32_16x16x32_f16 v[58:61], v[110:113], v[150:153], v[58:61]
	ds_read_b128 v[142:145], v163 offset:4096
	v_mfma_f32_16x16x32_f16 v[14:17], v[110:113], v[154:157], v[14:17]
	ds_read_b128 v[86:89], v159
	v_mfma_f32_16x16x32_f16 v[78:81], v[114:117], v[146:149], v[78:81]
	ds_read_b128 v[90:93], v159 offset:2048
	v_mfma_f32_16x16x32_f16 v[22:25], v[114:117], v[150:153], v[22:25]
	ds_read_b128 v[94:97], v159 offset:4096
	v_mfma_f32_16x16x32_f16 v[30:33], v[114:117], v[154:157], v[30:33]
	ds_read_b128 v[98:101], v159 offset:6144
	v_mfma_f32_16x16x32_f16 v[74:77], v[118:121], v[146:149], v[74:77]
	ds_read_b128 v[102:105], v159 offset:8192
	v_mfma_f32_16x16x32_f16 v[18:21], v[118:121], v[150:153], v[18:21]
	ds_read_b128 v[106:109], v159 offset:10240
	v_mfma_f32_16x16x32_f16 v[26:29], v[118:121], v[154:157], v[26:29]
	v_mfma_f32_16x16x32_f16 v[70:73], v[122:125], v[146:149], v[70:73]
	v_mfma_f32_16x16x32_f16 v[46:49], v[122:125], v[150:153], v[46:49]
	v_mfma_f32_16x16x32_f16 v[240:243], v[122:125], v[154:157], v[240:243]
	v_mfma_f32_16x16x32_f16 v[66:69], v[126:129], v[146:149], v[66:69]
	v_mfma_f32_16x16x32_f16 v[42:45], v[126:129], v[150:153], v[42:45]
	v_mfma_f32_16x16x32_f16 v[236:239], v[126:129], v[154:157], v[236:239]
	v_mfma_f32_16x16x32_f16 v[62:65], v[130:133], v[146:149], v[62:65]
	v_mfma_f32_16x16x32_f16 v[38:41], v[130:133], v[150:153], v[38:41]
	v_mfma_f32_16x16x32_f16 v[34:37], v[130:133], v[154:157], v[34:37]
	s_waitcnt lgkmcnt(0)
	ds_read_b128 v[146:149], v165
	v_mfma_f32_16x16x32_f16 v[82:85], v[86:89], v[134:137], v[82:85]
	ds_read_b128 v[150:153], v165 offset:2048
	v_mfma_f32_16x16x32_f16 v[58:61], v[86:89], v[138:141], v[58:61]
	ds_read_b128 v[154:157], v165 offset:4096
	v_mfma_f32_16x16x32_f16 v[14:17], v[86:89], v[142:145], v[14:17]
	ds_read_b128 v[110:113], v161
	v_mfma_f32_16x16x32_f16 v[78:81], v[90:93], v[134:137], v[78:81]
	ds_read_b128 v[114:117], v161 offset:2048
	v_mfma_f32_16x16x32_f16 v[22:25], v[90:93], v[138:141], v[22:25]
	ds_read_b128 v[118:121], v161 offset:4096
	v_mfma_f32_16x16x32_f16 v[30:33], v[90:93], v[142:145], v[30:33]
	ds_read_b128 v[122:125], v161 offset:6144
	v_mfma_f32_16x16x32_f16 v[74:77], v[94:97], v[134:137], v[74:77]
	ds_read_b128 v[126:129], v161 offset:8192
	v_mfma_f32_16x16x32_f16 v[18:21], v[94:97], v[138:141], v[18:21]
	ds_read_b128 v[130:133], v161 offset:10240
	v_mfma_f32_16x16x32_f16 v[26:29], v[94:97], v[142:145], v[26:29]
	v_mfma_f32_16x16x32_f16 v[70:73], v[98:101], v[134:137], v[70:73]
	v_mfma_f32_16x16x32_f16 v[46:49], v[98:101], v[138:141], v[46:49]
	v_mfma_f32_16x16x32_f16 v[240:243], v[98:101], v[142:145], v[240:243]
	v_mfma_f32_16x16x32_f16 v[66:69], v[102:105], v[134:137], v[66:69]
	v_mfma_f32_16x16x32_f16 v[42:45], v[102:105], v[138:141], v[42:45]
	v_mfma_f32_16x16x32_f16 v[236:239], v[102:105], v[142:145], v[236:239]
	v_mfma_f32_16x16x32_f16 v[62:65], v[106:109], v[134:137], v[62:65]
	v_mfma_f32_16x16x32_f16 v[38:41], v[106:109], v[138:141], v[38:41]
	v_mfma_f32_16x16x32_f16 v[34:37], v[106:109], v[142:145], v[34:37]
	s_waitcnt vmcnt(3) lgkmcnt(0)
	s_barrier
	ds_read_b128 v[134:137], v162
	v_mfma_f32_16x16x32_f16 v[82:85], v[110:113], v[146:149], v[82:85]
	ds_read_b128 v[138:141], v162 offset:2048
	v_mfma_f32_16x16x32_f16 v[58:61], v[110:113], v[150:153], v[58:61]
	ds_read_b128 v[142:145], v162 offset:4096
	v_mfma_f32_16x16x32_f16 v[14:17], v[110:113], v[154:157], v[14:17]
	ds_read_b128 v[86:89], v158
	v_mfma_f32_16x16x32_f16 v[78:81], v[114:117], v[146:149], v[78:81]
	ds_read_b128 v[90:93], v158 offset:2048
	v_mfma_f32_16x16x32_f16 v[22:25], v[114:117], v[150:153], v[22:25]
	ds_read_b128 v[94:97], v158 offset:4096
	v_mfma_f32_16x16x32_f16 v[30:33], v[114:117], v[154:157], v[30:33]
	ds_read_b128 v[98:101], v158 offset:6144
	v_mfma_f32_16x16x32_f16 v[74:77], v[118:121], v[146:149], v[74:77]
	ds_read_b128 v[102:105], v158 offset:8192
	v_mfma_f32_16x16x32_f16 v[18:21], v[118:121], v[150:153], v[18:21]
	ds_read_b128 v[106:109], v158 offset:10240
	v_mfma_f32_16x16x32_f16 v[26:29], v[118:121], v[154:157], v[26:29]
	v_mfma_f32_16x16x32_f16 v[70:73], v[122:125], v[146:149], v[70:73]
	v_mfma_f32_16x16x32_f16 v[46:49], v[122:125], v[150:153], v[46:49]
	v_mfma_f32_16x16x32_f16 v[240:243], v[122:125], v[154:157], v[240:243]
	v_mfma_f32_16x16x32_f16 v[66:69], v[126:129], v[146:149], v[66:69]
	v_mfma_f32_16x16x32_f16 v[42:45], v[126:129], v[150:153], v[42:45]
	v_mfma_f32_16x16x32_f16 v[236:239], v[126:129], v[154:157], v[236:239]
	v_mfma_f32_16x16x32_f16 v[62:65], v[130:133], v[146:149], v[62:65]
	v_mfma_f32_16x16x32_f16 v[38:41], v[130:133], v[150:153], v[38:41]
	v_mfma_f32_16x16x32_f16 v[34:37], v[130:133], v[154:157], v[34:37]
	s_waitcnt lgkmcnt(0)
	ds_read_b128 v[146:149], v164
	v_mfma_f32_16x16x32_f16 v[82:85], v[86:89], v[134:137], v[82:85]
	ds_read_b128 v[150:153], v164 offset:2048
	v_mfma_f32_16x16x32_f16 v[58:61], v[86:89], v[138:141], v[58:61]
	ds_read_b128 v[154:157], v164 offset:4096
	v_mfma_f32_16x16x32_f16 v[14:17], v[86:89], v[142:145], v[14:17]
	ds_read_b128 v[110:113], v160
	v_mfma_f32_16x16x32_f16 v[78:81], v[90:93], v[134:137], v[78:81]
	ds_read_b128 v[114:117], v160 offset:2048
	v_mfma_f32_16x16x32_f16 v[22:25], v[90:93], v[138:141], v[22:25]
	ds_read_b128 v[118:121], v160 offset:4096
	v_mfma_f32_16x16x32_f16 v[30:33], v[90:93], v[142:145], v[30:33]
	ds_read_b128 v[122:125], v160 offset:6144
	v_mfma_f32_16x16x32_f16 v[74:77], v[94:97], v[134:137], v[74:77]
	ds_read_b128 v[126:129], v160 offset:8192
	v_mfma_f32_16x16x32_f16 v[18:21], v[94:97], v[138:141], v[18:21]
	ds_read_b128 v[130:133], v160 offset:10240
	v_mfma_f32_16x16x32_f16 v[26:29], v[94:97], v[142:145], v[26:29]
	v_mfma_f32_16x16x32_f16 v[70:73], v[98:101], v[134:137], v[70:73]
	v_mfma_f32_16x16x32_f16 v[46:49], v[98:101], v[138:141], v[46:49]
	v_mfma_f32_16x16x32_f16 v[240:243], v[98:101], v[142:145], v[240:243]
	v_mfma_f32_16x16x32_f16 v[66:69], v[102:105], v[134:137], v[66:69]
	v_mfma_f32_16x16x32_f16 v[42:45], v[102:105], v[138:141], v[42:45]
	v_mfma_f32_16x16x32_f16 v[236:239], v[102:105], v[142:145], v[236:239]
	v_mfma_f32_16x16x32_f16 v[62:65], v[106:109], v[134:137], v[62:65]
	v_mfma_f32_16x16x32_f16 v[38:41], v[106:109], v[138:141], v[38:41]
	v_mfma_f32_16x16x32_f16 v[34:37], v[106:109], v[142:145], v[34:37]
	s_waitcnt lgkmcnt(0)
	v_mfma_f32_16x16x32_f16 v[82:85], v[110:113], v[146:149], v[82:85]
	v_mfma_f32_16x16x32_f16 v[58:61], v[110:113], v[150:153], v[58:61]
	v_mfma_f32_16x16x32_f16 v[14:17], v[110:113], v[154:157], v[14:17]
	v_mfma_f32_16x16x32_f16 v[78:81], v[114:117], v[146:149], v[78:81]
	v_mfma_f32_16x16x32_f16 v[22:25], v[114:117], v[150:153], v[22:25]
	v_mfma_f32_16x16x32_f16 v[30:33], v[114:117], v[154:157], v[30:33]
	v_mfma_f32_16x16x32_f16 v[74:77], v[118:121], v[146:149], v[74:77]
	v_mfma_f32_16x16x32_f16 v[18:21], v[118:121], v[150:153], v[18:21]
	v_mfma_f32_16x16x32_f16 v[26:29], v[118:121], v[154:157], v[26:29]
	v_mfma_f32_16x16x32_f16 v[70:73], v[122:125], v[146:149], v[70:73]
	v_mfma_f32_16x16x32_f16 v[46:49], v[122:125], v[150:153], v[46:49]
	v_mfma_f32_16x16x32_f16 v[240:243], v[122:125], v[154:157], v[240:243]
	v_mfma_f32_16x16x32_f16 v[66:69], v[126:129], v[146:149], v[66:69]
	v_mfma_f32_16x16x32_f16 v[42:45], v[126:129], v[150:153], v[42:45]
	v_mfma_f32_16x16x32_f16 v[236:239], v[126:129], v[154:157], v[236:239]
	v_mfma_f32_16x16x32_f16 v[62:65], v[130:133], v[146:149], v[62:65]
	v_mfma_f32_16x16x32_f16 v[38:41], v[130:133], v[150:153], v[38:41]
	v_mfma_f32_16x16x32_f16 v[34:37], v[130:133], v[154:157], v[34:37]
